# v35 + hand-written top-3 update in MoBA routing (compares + med3/max + selects instead of the branchy exec-masked insert; same result because a lane sees its candidate blocks in increasing index order
# speedup vs baseline: 1.0194x; 1.0069x over previous
.Lmb_tail:
	s_add_i32 s12, s12, -1
	v_add_u32_e32 v73, 32, v73
	s_cmp_eq_u32 s12, 0
	v_add_u32_e32 v72, 0x2200, v72
	s_cbranch_scc1 .LBB0_1053
.LBB0_830:
	ds_read_b128 v[2:5], v72
	ds_read_b128 v[74:77], v72 offset:32
	ds_read_b128 v[78:81], v72 offset:17408
	ds_read_b128 v[82:85], v72 offset:17440
	v_cmp_gt_i32_e32 vcc, s39, v73
	s_waitcnt lgkmcnt(3)
	v_mfma_f32_32x32x16_bf16 v[2:17], v[2:5], v[42:45], 0
	s_waitcnt lgkmcnt(1)
	v_mfma_f32_32x32x16_bf16 v[2:17], v[78:81], v[42:45], v[2:17]
	v_mfma_f32_32x32x16_bf16 v[2:17], v[74:77], v[18:21], v[2:17]
	ds_read_b128 v[74:77], v72 offset:64
	ds_read_b128 v[78:81], v72 offset:96
	s_waitcnt lgkmcnt(2)
	v_mfma_f32_32x32x16_bf16 v[2:17], v[82:85], v[18:21], v[2:17]
	s_waitcnt lgkmcnt(1)
	v_mfma_f32_32x32x16_bf16 v[2:17], v[74:77], v[22:25], v[2:17]
	ds_read_b128 v[74:77], v72 offset:17472
	ds_read_b128 v[82:85], v72 offset:17504
	s_waitcnt lgkmcnt(1)
	v_mfma_f32_32x32x16_bf16 v[2:17], v[74:77], v[22:25], v[2:17]
	v_mfma_f32_32x32x16_bf16 v[2:17], v[78:81], v[26:29], v[2:17]
	ds_read_b128 v[74:77], v72 offset:128
	ds_read_b128 v[78:81], v72 offset:160
	s_waitcnt lgkmcnt(2)
	v_mfma_f32_32x32x16_bf16 v[2:17], v[82:85], v[26:29], v[2:17]
	s_waitcnt lgkmcnt(1)
	v_mfma_f32_32x32x16_bf16 v[2:17], v[74:77], v[30:33], v[2:17]
	ds_read_b128 v[74:77], v72 offset:17536
	ds_read_b128 v[82:85], v72 offset:17568
	s_waitcnt lgkmcnt(1)
	v_mfma_f32_32x32x16_bf16 v[2:17], v[74:77], v[30:33], v[2:17]
	v_mfma_f32_32x32x16_bf16 v[2:17], v[78:81], v[34:37], v[2:17]
	ds_read_b128 v[74:77], v72 offset:192
	ds_read_b128 v[78:81], v72 offset:224
	s_waitcnt lgkmcnt(2)
	v_mfma_f32_32x32x16_bf16 v[2:17], v[82:85], v[34:37], v[2:17]
	s_waitcnt lgkmcnt(1)
	v_mfma_f32_32x32x16_bf16 v[2:17], v[74:77], v[38:41], v[2:17]
	ds_read_b128 v[74:77], v72 offset:17600
	ds_read_b128 v[82:85], v72 offset:17632
	s_waitcnt lgkmcnt(1)
	v_mfma_f32_32x32x16_bf16 v[2:17], v[74:77], v[38:41], v[2:17]
	v_mfma_f32_32x32x16_bf16 v[2:17], v[78:81], v[46:49], v[2:17]
	s_waitcnt lgkmcnt(0)
	v_mfma_f32_32x32x16_bf16 v[2:17], v[82:85], v[46:49], v[2:17]
	s_nop 15
	v_mov_b32_e32 v76, 0xff800000
	v_cmp_gt_i32_e32 vcc, s39, v73
	s_nop 1
	v_cndmask_b32_e32 v2, v76, v2, vcc
	v_cmp_gt_f32_e64 s[20:21], v2, v71
	v_cmp_gt_f32_e64 s[22:23], v2, v50
	v_cmp_gt_f32_e64 s[24:25], v2, v57
	v_med3_f32 v57, v50, v2, v57
	v_med3_f32 v50, v71, v2, v50
	v_max_f32_e32 v71, v71, v2
	v_cndmask_b32_e64 v75, v70, v73, s[24:25]
	v_cndmask_b32_e64 v70, v75, v59, s[22:23]
	v_cndmask_b32_e64 v75, v59, v73, s[22:23]
	v_cndmask_b32_e64 v59, v75, v69, s[20:21]
	v_cndmask_b32_e64 v69, v69, v73, s[20:21]
	v_add_u32_e32 v74, 1, v73
	v_cmp_gt_i32_e32 vcc, s39, v74
	s_nop 1
	v_cndmask_b32_e32 v3, v76, v3, vcc
	v_cmp_gt_f32_e64 s[20:21], v3, v71
	v_cmp_gt_f32_e64 s[22:23], v3, v50
	v_cmp_gt_f32_e64 s[24:25], v3, v57
	v_med3_f32 v57, v50, v3, v57
	v_med3_f32 v50, v71, v3, v50
	v_max_f32_e32 v71, v71, v3
	v_cndmask_b32_e64 v75, v70, v74, s[24:25]
	v_cndmask_b32_e64 v70, v75, v59, s[22:23]
	v_cndmask_b32_e64 v75, v59, v74, s[22:23]
	v_cndmask_b32_e64 v59, v75, v69, s[20:21]
	v_cndmask_b32_e64 v69, v69, v74, s[20:21]
	v_add_u32_e32 v74, 2, v73
	v_cmp_gt_i32_e32 vcc, s39, v74
	s_nop 1
	v_cndmask_b32_e32 v4, v76, v4, vcc
	v_cmp_gt_f32_e64 s[20:21], v4, v71
	v_cmp_gt_f32_e64 s[22:23], v4, v50
	v_cmp_gt_f32_e64 s[24:25], v4, v57
	v_med3_f32 v57, v50, v4, v57
	v_med3_f32 v50, v71, v4, v50
	v_max_f32_e32 v71, v71, v4
	v_cndmask_b32_e64 v75, v70, v74, s[24:25]
	v_cndmask_b32_e64 v70, v75, v59, s[22:23]
	v_cndmask_b32_e64 v75, v59, v74, s[22:23]
	v_cndmask_b32_e64 v59, v75, v69, s[20:21]
	v_cndmask_b32_e64 v69, v69, v74, s[20:21]
	v_add_u32_e32 v74, 3, v73
	v_cmp_gt_i32_e32 vcc, s39, v74
	s_nop 1
	v_cndmask_b32_e32 v5, v76, v5, vcc
	v_cmp_gt_f32_e64 s[20:21], v5, v71
	v_cmp_gt_f32_e64 s[22:23], v5, v50
	v_cmp_gt_f32_e64 s[24:25], v5, v57
	v_med3_f32 v57, v50, v5, v57
	v_med3_f32 v50, v71, v5, v50
	v_max_f32_e32 v71, v71, v5
	v_cndmask_b32_e64 v75, v70, v74, s[24:25]
	v_cndmask_b32_e64 v70, v75, v59, s[22:23]
	v_cndmask_b32_e64 v75, v59, v74, s[22:23]
	v_cndmask_b32_e64 v59, v75, v69, s[20:21]
	v_cndmask_b32_e64 v69, v69, v74, s[20:21]
	v_add_u32_e32 v74, 8, v73
	v_cmp_gt_i32_e32 vcc, s39, v74
	s_nop 1
	v_cndmask_b32_e32 v6, v76, v6, vcc
	v_cmp_gt_f32_e64 s[20:21], v6, v71
	v_cmp_gt_f32_e64 s[22:23], v6, v50
	v_cmp_gt_f32_e64 s[24:25], v6, v57
	v_med3_f32 v57, v50, v6, v57
	v_med3_f32 v50, v71, v6, v50
	v_max_f32_e32 v71, v71, v6
	v_cndmask_b32_e64 v75, v70, v74, s[24:25]
	v_cndmask_b32_e64 v70, v75, v59, s[22:23]
	v_cndmask_b32_e64 v75, v59, v74, s[22:23]
	v_cndmask_b32_e64 v59, v75, v69, s[20:21]
	v_cndmask_b32_e64 v69, v69, v74, s[20:21]
	v_add_u32_e32 v74, 9, v73
	v_cmp_gt_i32_e32 vcc, s39, v74
	s_nop 1
	v_cndmask_b32_e32 v7, v76, v7, vcc
	v_cmp_gt_f32_e64 s[20:21], v7, v71
	v_cmp_gt_f32_e64 s[22:23], v7, v50
	v_cmp_gt_f32_e64 s[24:25], v7, v57
	v_med3_f32 v57, v50, v7, v57
	v_med3_f32 v50, v71, v7, v50
	v_max_f32_e32 v71, v71, v7
	v_cndmask_b32_e64 v75, v70, v74, s[24:25]
	v_cndmask_b32_e64 v70, v75, v59, s[22:23]
	v_cndmask_b32_e64 v75, v59, v74, s[22:23]
	v_cndmask_b32_e64 v59, v75, v69, s[20:21]
	v_cndmask_b32_e64 v69, v69, v74, s[20:21]
	v_add_u32_e32 v74, 10, v73
	v_cmp_gt_i32_e32 vcc, s39, v74
	s_nop 1
	v_cndmask_b32_e32 v8, v76, v8, vcc
	v_cmp_gt_f32_e64 s[20:21], v8, v71
	v_cmp_gt_f32_e64 s[22:23], v8, v50
	v_cmp_gt_f32_e64 s[24:25], v8, v57
	v_med3_f32 v57, v50, v8, v57
	v_med3_f32 v50, v71, v8, v50
	v_max_f32_e32 v71, v71, v8
	v_cndmask_b32_e64 v75, v70, v74, s[24:25]
	v_cndmask_b32_e64 v70, v75, v59, s[22:23]
	v_cndmask_b32_e64 v75, v59, v74, s[22:23]
	v_cndmask_b32_e64 v59, v75, v69, s[20:21]
	v_cndmask_b32_e64 v69, v69, v74, s[20:21]
	v_add_u32_e32 v74, 11, v73
	v_cmp_gt_i32_e32 vcc, s39, v74
	s_nop 1
	v_cndmask_b32_e32 v9, v76, v9, vcc
	v_cmp_gt_f32_e64 s[20:21], v9, v71
	v_cmp_gt_f32_e64 s[22:23], v9, v50
	v_cmp_gt_f32_e64 s[24:25], v9, v57
	v_med3_f32 v57, v50, v9, v57
	v_med3_f32 v50, v71, v9, v50
	v_max_f32_e32 v71, v71, v9
	v_cndmask_b32_e64 v75, v70, v74, s[24:25]
	v_cndmask_b32_e64 v70, v75, v59, s[22:23]
	v_cndmask_b32_e64 v75, v59, v74, s[22:23]
	v_cndmask_b32_e64 v59, v75, v69, s[20:21]
	v_cndmask_b32_e64 v69, v69, v74, s[20:21]
	v_add_u32_e32 v74, 16, v73
	v_cmp_gt_i32_e32 vcc, s39, v74
	s_nop 1
	v_cndmask_b32_e32 v10, v76, v10, vcc
	v_cmp_gt_f32_e64 s[20:21], v10, v71
	v_cmp_gt_f32_e64 s[22:23], v10, v50
	v_cmp_gt_f32_e64 s[24:25], v10, v57
	v_med3_f32 v57, v50, v10, v57
	v_med3_f32 v50, v71, v10, v50
	v_max_f32_e32 v71, v71, v10
	v_cndmask_b32_e64 v75, v70, v74, s[24:25]
	v_cndmask_b32_e64 v70, v75, v59, s[22:23]
	v_cndmask_b32_e64 v75, v59, v74, s[22:23]
	v_cndmask_b32_e64 v59, v75, v69, s[20:21]
	v_cndmask_b32_e64 v69, v69, v74, s[20:21]
	v_add_u32_e32 v74, 17, v73
	v_cmp_gt_i32_e32 vcc, s39, v74
	s_nop 1
	v_cndmask_b32_e32 v11, v76, v11, vcc
	v_cmp_gt_f32_e64 s[20:21], v11, v71
	v_cmp_gt_f32_e64 s[22:23], v11, v50
	v_cmp_gt_f32_e64 s[24:25], v11, v57
	v_med3_f32 v57, v50, v11, v57
	v_med3_f32 v50, v71, v11, v50
	v_max_f32_e32 v71, v71, v11
	v_cndmask_b32_e64 v75, v70, v74, s[24:25]
	v_cndmask_b32_e64 v70, v75, v59, s[22:23]
	v_cndmask_b32_e64 v75, v59, v74, s[22:23]
	v_cndmask_b32_e64 v59, v75, v69, s[20:21]
	v_cndmask_b32_e64 v69, v69, v74, s[20:21]
	v_add_u32_e32 v74, 18, v73
	v_cmp_gt_i32_e32 vcc, s39, v74
	s_nop 1
	v_cndmask_b32_e32 v12, v76, v12, vcc
	v_cmp_gt_f32_e64 s[20:21], v12, v71
	v_cmp_gt_f32_e64 s[22:23], v12, v50
	v_cmp_gt_f32_e64 s[24:25], v12, v57
	v_med3_f32 v57, v50, v12, v57
	v_med3_f32 v50, v71, v12, v50
	v_max_f32_e32 v71, v71, v12
	v_cndmask_b32_e64 v75, v70, v74, s[24:25]
	v_cndmask_b32_e64 v70, v75, v59, s[22:23]
	v_cndmask_b32_e64 v75, v59, v74, s[22:23]
	v_cndmask_b32_e64 v59, v75, v69, s[20:21]
	v_cndmask_b32_e64 v69, v69, v74, s[20:21]
	v_add_u32_e32 v74, 19, v73
	v_cmp_gt_i32_e32 vcc, s39, v74
	s_nop 1
	v_cndmask_b32_e32 v13, v76, v13, vcc
	v_cmp_gt_f32_e64 s[20:21], v13, v71
	v_cmp_gt_f32_e64 s[22:23], v13, v50
	v_cmp_gt_f32_e64 s[24:25], v13, v57
	v_med3_f32 v57, v50, v13, v57
	v_med3_f32 v50, v71, v13, v50
	v_max_f32_e32 v71, v71, v13
	v_cndmask_b32_e64 v75, v70, v74, s[24:25]
	v_cndmask_b32_e64 v70, v75, v59, s[22:23]
	v_cndmask_b32_e64 v75, v59, v74, s[22:23]
	v_cndmask_b32_e64 v59, v75, v69, s[20:21]
	v_cndmask_b32_e64 v69, v69, v74, s[20:21]
	v_add_u32_e32 v74, 24, v73
	v_cmp_gt_i32_e32 vcc, s39, v74
	s_nop 1
	v_cndmask_b32_e32 v14, v76, v14, vcc
	v_cmp_gt_f32_e64 s[20:21], v14, v71
	v_cmp_gt_f32_e64 s[22:23], v14, v50
	v_cmp_gt_f32_e64 s[24:25], v14, v57
	v_med3_f32 v57, v50, v14, v57
	v_med3_f32 v50, v71, v14, v50
	v_max_f32_e32 v71, v71, v14
	v_cndmask_b32_e64 v75, v70, v74, s[24:25]
	v_cndmask_b32_e64 v70, v75, v59, s[22:23]
	v_cndmask_b32_e64 v75, v59, v74, s[22:23]
	v_cndmask_b32_e64 v59, v75, v69, s[20:21]
	v_cndmask_b32_e64 v69, v69, v74, s[20:21]
	v_add_u32_e32 v74, 25, v73
	v_cmp_gt_i32_e32 vcc, s39, v74
	s_nop 1
	v_cndmask_b32_e32 v15, v76, v15, vcc
	v_cmp_gt_f32_e64 s[20:21], v15, v71
	v_cmp_gt_f32_e64 s[22:23], v15, v50
	v_cmp_gt_f32_e64 s[24:25], v15, v57
	v_med3_f32 v57, v50, v15, v57
	v_med3_f32 v50, v71, v15, v50
	v_max_f32_e32 v71, v71, v15
	v_cndmask_b32_e64 v75, v70, v74, s[24:25]
	v_cndmask_b32_e64 v70, v75, v59, s[22:23]
	v_cndmask_b32_e64 v75, v59, v74, s[22:23]
	v_cndmask_b32_e64 v59, v75, v69, s[20:21]
	v_cndmask_b32_e64 v69, v69, v74, s[20:21]
	v_add_u32_e32 v74, 26, v73
	v_cmp_gt_i32_e32 vcc, s39, v74
	s_nop 1
	v_cndmask_b32_e32 v16, v76, v16, vcc
	v_cmp_gt_f32_e64 s[20:21], v16, v71
	v_cmp_gt_f32_e64 s[22:23], v16, v50
	v_cmp_gt_f32_e64 s[24:25], v16, v57
	v_med3_f32 v57, v50, v16, v57
	v_med3_f32 v50, v71, v16, v50
	v_max_f32_e32 v71, v71, v16
	v_cndmask_b32_e64 v75, v70, v74, s[24:25]
	v_cndmask_b32_e64 v70, v75, v59, s[22:23]
	v_cndmask_b32_e64 v75, v59, v74, s[22:23]
	v_cndmask_b32_e64 v59, v75, v69, s[20:21]
	v_cndmask_b32_e64 v69, v69, v74, s[20:21]
	v_add_u32_e32 v74, 27, v73
	v_cmp_gt_i32_e32 vcc, s39, v74
	s_nop 1
	v_cndmask_b32_e32 v17, v76, v17, vcc
	v_cmp_gt_f32_e64 s[20:21], v17, v71
	v_cmp_gt_f32_e64 s[22:23], v17, v50
	v_cmp_gt_f32_e64 s[24:25], v17, v57
	v_med3_f32 v57, v50, v17, v57
	v_med3_f32 v50, v71, v17, v50
	v_max_f32_e32 v71, v71, v17
	v_cndmask_b32_e64 v75, v70, v74, s[24:25]
	v_cndmask_b32_e64 v70, v75, v59, s[22:23]
	v_cndmask_b32_e64 v75, v59, v74, s[22:23]
	v_cndmask_b32_e64 v59, v75, v69, s[20:21]
	v_cndmask_b32_e64 v69, v69, v74, s[20:21]
	s_branch .Lmb_tail

.LBB0_1053:
	s_nop 0
	v_and_b32_e32 v3, 64, v68
	v_xor_b32_e32 v2, 32, v68
	v_add_u32_e32 v3, 64, v3
	v_cmp_lt_i32_e32 vcc, v2, v3
	s_mov_b64 s[20:21], -1
	s_mov_b64 s[22:23], -1
	v_cndmask_b32_e32 v2, v68, v2, vcc
	v_lshlrev_b32_e32 v2, 2, v2
	ds_bpermute_b32 v6, v2, v71
	ds_bpermute_b32 v5, v2, v50
	ds_bpermute_b32 v3, v2, v57
	ds_bpermute_b32 v7, v2, v69
	ds_bpermute_b32 v4, v2, v59
	ds_bpermute_b32 v2, v2, v70
	s_waitcnt lgkmcnt(5)
	v_cmp_nlt_f32_e32 vcc, v71, v6
	s_and_saveexec_b64 s[18:19], vcc
	s_cbranch_execz .LBB0_1057
	v_cmp_eq_f32_e32 vcc, v71, v6
	s_mov_b64 s[22:23], 0
	s_and_saveexec_b64 s[24:25], vcc
	s_cbranch_execz .LBB0_1056
	s_waitcnt lgkmcnt(2)
	v_cmp_lt_i32_e32 vcc, v7, v69
	s_and_b64 s[22:23], vcc, exec
